# grid barrier: first-arriving workgroup per XCD starts one early L2 write-back
# speedup vs baseline: 1.0002x; 1.0002x over previous
.LBB0_116:
	v_readlane_b32 s2, v255, 21
	s_lshl_b32 s2, s2, 8
	v_readlane_b32 s4, v255, 19
	v_readlane_b32 s5, v255, 20
	s_add_u32 s2, s4, s2
	s_addc_u32 s3, s5, 0
	v_mov_b32_e32 v2, 0x1000
	v_mov_b32_e32 v4, 1
	global_atomic_add v4, v2, v4, s[2:3] offset:1024 sc0
	v_cvt_f32_u32_e32 v2, v3
	v_sub_u32_e32 v5, 0, v3
	v_rcp_iflag_f32_e32 v2, v2
	s_nop 0
	v_mul_f32_e32 v2, 0x4f7ffffe, v2
	v_cvt_u32_f32_e32 v2, v2
	v_mul_lo_u32 v5, v5, v2
	v_mul_hi_u32 v5, v2, v5
	v_add_u32_e32 v2, v2, v5
	s_waitcnt vmcnt(0)
	v_mul_hi_u32 v2, v4, v2
	v_mul_lo_u32 v5, v2, v3
	v_sub_u32_e32 v5, v4, v5
	v_add_u32_e32 v6, 1, v2
	v_cmp_ge_u32_e32 vcc, v5, v3
	v_add_u32_e32 v4, 1, v4
	s_nop 0
	v_cndmask_b32_e32 v2, v2, v6, vcc
	v_sub_u32_e32 v6, v5, v3
	v_cndmask_b32_e32 v5, v5, v6, vcc
	v_add_u32_e32 v6, 1, v2
	v_cmp_ge_u32_e32 vcc, v5, v3
	s_nop 1
	v_cndmask_b32_e32 v2, v2, v6, vcc
	v_mul_lo_u32 v5, v3, v2
	v_add_u32_e32 v3, v5, v3
	v_cmp_ne_u32_e32 vcc, v4, v3
	s_and_saveexec_b64 s[4:5], vcc
	s_xor_b64 s[4:5], exec, s[4:5]
	s_cbranch_execz .LBB0_130
	s_waitcnt lgkmcnt(0)
	v_add_u32_e32 v6, 1, v5
	v_cmp_eq_u32_e32 vcc, v4, v6
	s_and_b64 vcc, exec, vcc
	s_cbranch_vccz .Lbarfw_0
	buffer_wbl2 sc1
.Lbarfw_0:
	v_mov_b32_e32 v1, 0x2000
	global_load_dword v1, v1, s[2:3] offset:1024 sc1
	s_add_u32 s10, s2, 0x2400
	s_addc_u32 s11, s3, 0
	s_waitcnt vmcnt(0)
	v_cmp_eq_u32_e32 vcc, v1, v2
	s_and_saveexec_b64 s[6:7], vcc
	s_cbranch_execz .LBB0_129
	s_add_u32 s8, s92, 0x4200
	s_addc_u32 s9, s93, 0
	s_mov_b32 s22, 1
	s_mov_b64 s[12:13], 0
	v_mov_b32_e32 v1, 0
	s_branch .LBB0_120
